# M2: non-temporal policy on the A-operand (expert hidden rows, read once) LDS-DMA loads so the yslot output stays in the infinity cache for N2
# baseline (speedup 1.0000x reference)
; #define PG8_STAGE_B(bufoff, gbase) PG8_STAGE_U(bufoff, gbase, voffB, qstepB)
; #define PG8_STAGE_A(bufoff, gbase, h, GO) do { if constexpr (GATHER) { PG8_STAGE(bufoff, gbase, (GO)[h]); } else { PG8_STAGE_U(bufoff, (const char*)(gbase) + (h) * hstepA, voffA, qstepA); } } while (0)
; #define PG8_LDA(dst, b, h) do { _Pragma("unroll") for (int m = 0; m < 4; ++m) _Pragma("unroll") for (int k = 0; k < 2; ++k) dst[m][k] = *(const LAS bf16x8*)(lds + PG8_SA(b, h) + aoff + m * 2048 + k * 1024); } while (0)
; #define PG8_LDB(dst, b, h) do { _Pragma("unroll") for (int n = 0; n < 2; ++n) _Pragma("unroll") for (int k = 0; k < 2; ++k) dst[n][k] = *(const LAS bf16x8*)(lds + PG8_SB(b, h) + boff + n * 2048 + k * 1024); } while (0)
; #define PG8_WAIT_V(n) asm volatile("s_waitcnt vmcnt(" #n ")" ::: "memory")
; #define PG8_WAIT_L(n) asm volatile("s_waitcnt lgkmcnt(" #n ")" ::: "memory")
; #define PG8_BAR __builtin_amdgcn_s_barrier()
; #define PG8_SCHED __builtin_amdgcn_sched_barrier(0)
;     ...
;             PG8_LDB(B0, 0, 0); PG8_LDB(B1, 0, 1); PG8_SCHED; PG8_LDA(At, 0, 0); PG8_STAGE_A(PG8_SA(1, 1), a1, 1, gc);
;             if constexpr (GATHER) { if (last && has_next) {
; #pragma unroll
;                 for (int h = 0; h < 2; ++h)
; #pragma unroll
;                     for (int i = 0; i < 2; ++i) { int _R, _C; stage_rc(tid * 16 + i * 8192, _R, _C); gc[h][i] = gn[h][i] * (unsigned)(lda * 2) + (unsigned)(_C * 2); } } }
;             PG8_WAIT_V(8); PG8_WAIT_L(0); PG8_BAR; if (cur.half != 2) { PG8_MMA(0, 0, At, B0); PG8_MMA(0, 1, At, B1); } PG8_BAR; PG8_SCHED;
;             PG8_LDA(At, 0, 1); PG8_STAGE_B(PG8_SB(0, 0), b2); PG8_STAGE_B(PG8_SB(0, 1), b2 + hstepB); PG8_STAGE_A(PG8_SA(0, 0), a2, 0, gc);
;             PG8_WAIT_V(8); PG8_WAIT_L(0); PG8_BAR; if (cur.half != 1) { PG8_MMA(1, 0, At, B0); PG8_MMA(1, 1, At, B1); } PG8_BAR; PG8_SCHED;
.LBB0_1318:
	v_add_u32_e32 v0, 0x10000, v216
	ds_read_b128 v[18:21], v0
	ds_read_b128 v[22:25], v0 offset:1024
	ds_read_b128 v[26:29], v0 offset:2048
	ds_read_b128 v[30:33], v0 offset:3072
	v_add_u32_e32 v0, 0x14000, v216
	ds_read_b128 v[2:5], v0
	ds_read_b128 v[6:9], v0 offset:1024
	ds_read_b128 v[10:13], v0 offset:2048
	ds_read_b128 v[14:17], v0 offset:3072
	s_add_u32 s4, s26, s30
	v_mov_b32_e32 v0, v214
	s_addc_u32 s5, s27, s31
	s_waitcnt lgkmcnt(0)
	ds_read_b128 v[58:61], v217
	ds_read_b128 v[62:65], v217 offset:1024
	ds_read_b128 v[50:53], v217 offset:2048
	ds_read_b128 v[54:57], v217 offset:3072
	ds_read_b128 v[42:45], v217 offset:4096
	ds_read_b128 v[46:49], v217 offset:5120
	ds_read_b128 v[34:37], v217 offset:6144
	ds_read_b128 v[38:41], v217 offset:7168
	s_add_i32 m0, s45, 0xc000
	v_lshl_add_u64 v[194:195], s[4:5], 0, v[0:1]
	v_lshl_add_u64 v[194:195], v[194:195], 0, s[88:89]
	v_mov_b32_e32 v0, v214
	global_load_lds_dwordx4 v[194:195], off nt
	s_add_i32 m0, s45, 0xe000
	v_lshl_add_u64 v[194:195], s[4:5], 0, v[0:1]
	v_lshl_add_u64 v[194:195], v[194:195], 0, s[90:91]
	global_load_lds_dwordx4 v[194:195], off nt
	s_waitcnt vmcnt(8)
	s_waitcnt lgkmcnt(0)
	v_cndmask_b32_e64 v0, 0, 1, s[34:35]
	v_cmp_ne_u32_e64 s[4:5], 1, v0
	s_andn2_b64 vcc, exec, s[34:35]
	s_barrier
	s_cbranch_vccnz .LBB0_1320
	s_setprio 1
	s_waitcnt lgkmcnt(0)
	v_mfma_f32_16x16x128_f8f6f4 v[190:193], v[18:25], v[58:65], v[190:193]
	v_mfma_f32_16x16x128_f8f6f4 v[186:189], v[26:33], v[58:65], v[186:189]
	v_mfma_f32_16x16x128_f8f6f4 v[182:185], v[18:25], v[50:57], v[182:185]
	v_mfma_f32_16x16x128_f8f6f4 v[178:181], v[26:33], v[50:57], v[178:181]
	v_mfma_f32_16x16x128_f8f6f4 v[158:161], v[18:25], v[42:49], v[158:161]
	v_mfma_f32_16x16x128_f8f6f4 v[154:157], v[26:33], v[42:49], v[154:157]
	v_mfma_f32_16x16x128_f8f6f4 v[150:153], v[18:25], v[34:41], v[150:153]
	v_mfma_f32_16x16x128_f8f6f4 v[146:149], v[26:33], v[34:41], v[146:149]
	s_setprio 0
	s_setprio 1
	v_mfma_f32_16x16x128_f8f6f4 v[174:177], v[2:9], v[58:65], v[174:177]
	v_mfma_f32_16x16x128_f8f6f4 v[170:173], v[10:17], v[58:65], v[170:173]
	v_mfma_f32_16x16x128_f8f6f4 v[166:169], v[2:9], v[50:57], v[166:169]
	v_mfma_f32_16x16x128_f8f6f4 v[162:165], v[10:17], v[50:57], v[162:165]
	v_mfma_f32_16x16x128_f8f6f4 v[142:145], v[2:9], v[42:49], v[142:145]
	v_mfma_f32_16x16x128_f8f6f4 v[138:141], v[10:17], v[42:49], v[138:141]
	v_mfma_f32_16x16x128_f8f6f4 v[134:137], v[2:9], v[34:41], v[134:137]
	v_mfma_f32_16x16x128_f8f6f4 v[130:133], v[10:17], v[34:41], v[130:133]
	s_setprio 0
.LBB0_1320:
	s_add_u32 s6, s26, s30
	s_addc_u32 s7, s27, s31
	s_add_u32 s6, s6, 0x100
	s_addc_u32 s7, s7, 0
	s_add_u32 s56, s3, s30
	s_addc_u32 s57, s60, s31
	s_cmpk_eq_i32 s30, 0x300
	s_cselect_b32 s43, s19, s7
	s_cselect_b32 s42, s58, s6
	s_cselect_b32 s57, s0, s57
	s_cselect_b32 s56, s1, s56
	s_barrier
	v_mov_b32_e32 v0, v215
	s_mov_b32 m0, s51
	s_waitcnt lgkmcnt(0)
	ds_read_b128 v[58:61], v217 offset:16384
	ds_read_b128 v[62:65], v217 offset:17408
	ds_read_b128 v[50:53], v217 offset:18432
	ds_read_b128 v[54:57], v217 offset:19456
	ds_read_b128 v[42:45], v217 offset:20480
	ds_read_b128 v[46:49], v217 offset:21504
	ds_read_b128 v[34:37], v217 offset:22528
	ds_read_b128 v[38:41], v217 offset:23552
	s_andn2_b64 vcc, exec, s[28:29]
	global_load_lds_dwordx4 v0, s[56:57]
	v_mov_b32_e32 v0, v215
	s_mov_b32 m0, s62
	v_lshl_add_u64 v[194:195], s[56:57], 0, v[0:1]
	v_lshl_add_u64 v[194:195], v[194:195], 0, s[74:75]
	v_mov_b32_e32 v0, v215
	global_load_lds_dwordx4 v[194:195], off
	s_mov_b32 m0, s63
	v_lshl_add_u64 v[194:195], s[56:57], 0, v[0:1]
	v_lshl_add_u64 v[194:195], v[194:195], 0, s[80:81]
	v_mov_b32_e32 v0, v215
	global_load_lds_dwordx4 v[194:195], off
	s_mov_b32 m0, s71
	v_lshl_add_u64 v[194:195], s[56:57], 0, v[0:1]
	v_lshl_add_u64 v[194:195], v[194:195], 0, s[82:83]
	v_mov_b32_e32 v0, v214
	global_load_lds_dwordx4 v[194:195], off
	s_mov_b32 m0, s45
	s_nop 0
	global_load_lds_dwordx4 v0, s[42:43] nt
	v_mov_b32_e32 v0, v214
	s_mov_b32 m0, s76
	v_lshl_add_u64 v[194:195], s[42:43], 0, v[0:1]
	v_lshl_add_u64 v[194:195], v[194:195], 0, s[74:75]
	global_load_lds_dwordx4 v[194:195], off nt
	s_waitcnt vmcnt(8)
	s_waitcnt lgkmcnt(0)
	v_cndmask_b32_e64 v0, 0, 1, s[28:29]
	v_cmp_ne_u32_e64 s[6:7], 1, v0
	s_barrier
	s_cbranch_vccnz .LBB0_1322
	s_setprio 1
	s_waitcnt lgkmcnt(0)
	v_mfma_f32_16x16x128_f8f6f4 v[126:129], v[18:25], v[58:65], v[126:129]
	v_mfma_f32_16x16x128_f8f6f4 v[122:125], v[26:33], v[58:65], v[122:125]
	v_mfma_f32_16x16x128_f8f6f4 v[118:121], v[18:25], v[50:57], v[118:121]
	v_mfma_f32_16x16x128_f8f6f4 v[114:117], v[26:33], v[50:57], v[114:117]
	v_mfma_f32_16x16x128_f8f6f4 v[94:97], v[18:25], v[42:49], v[94:97]
	v_mfma_f32_16x16x128_f8f6f4 v[90:93], v[26:33], v[42:49], v[90:93]
	v_mfma_f32_16x16x128_f8f6f4 v[86:89], v[18:25], v[34:41], v[86:89]
	v_mfma_f32_16x16x128_f8f6f4 v[82:85], v[26:33], v[34:41], v[82:85]
	s_setprio 0
	s_setprio 1
	v_mfma_f32_16x16x128_f8f6f4 v[110:113], v[2:9], v[58:65], v[110:113]
	v_mfma_f32_16x16x128_f8f6f4 v[106:109], v[10:17], v[58:65], v[106:109]
	v_mfma_f32_16x16x128_f8f6f4 v[102:105], v[2:9], v[50:57], v[102:105]
	v_mfma_f32_16x16x128_f8f6f4 v[98:101], v[10:17], v[50:57], v[98:101]
	v_mfma_f32_16x16x128_f8f6f4 v[78:81], v[2:9], v[42:49], v[78:81]
	v_mfma_f32_16x16x128_f8f6f4 v[74:77], v[10:17], v[42:49], v[74:77]
	v_mfma_f32_16x16x128_f8f6f4 v[70:73], v[2:9], v[34:41], v[70:73]
	v_mfma_f32_16x16x128_f8f6f4 v[66:69], v[10:17], v[34:41], v[66:69]
	s_setprio 0
; #define PG8_STAGE_B(bufoff, gbase) PG8_STAGE_U(bufoff, gbase, voffB, qstepB)
; #define PG8_STAGE_A(bufoff, gbase, h, GO) do { if constexpr (GATHER) { PG8_STAGE(bufoff, gbase, (GO)[h]); } else { PG8_STAGE_U(bufoff, (const char*)(gbase) + (h) * hstepA, voffA, qstepA); } } while (0)
; #define PG8_LDA(dst, b, h) do { _Pragma("unroll") for (int m = 0; m < 4; ++m) _Pragma("unroll") for (int k = 0; k < 2; ++k) dst[m][k] = *(const LAS bf16x8*)(lds + PG8_SA(b, h) + aoff + m * 2048 + k * 1024); } while (0)
; #define PG8_LDB(dst, b, h) do { _Pragma("unroll") for (int n = 0; n < 2; ++n) _Pragma("unroll") for (int k = 0; k < 2; ++k) dst[n][k] = *(const LAS bf16x8*)(lds + PG8_SB(b, h) + boff + n * 2048 + k * 1024); } while (0)
; #define PG8_WAIT_V(n) asm volatile("s_waitcnt vmcnt(" #n ")" ::: "memory")
; #define PG8_WAIT_L(n) asm volatile("s_waitcnt lgkmcnt(" #n ")" ::: "memory")
; #define PG8_BAR __builtin_amdgcn_s_barrier()
; #define PG8_SCHED __builtin_amdgcn_sched_barrier(0)
;     ...
;             PG8_LDB(B0, 1, 0); PG8_LDB(B1, 1, 1); PG8_SCHED; PG8_LDA(At, 1, 0); PG8_STAGE_A(PG8_SA(0, 1), a2, 1, gc);
;             PG8_WAIT_V(8); PG8_WAIT_L(0); PG8_BAR; if (cur.half != 2) { PG8_MMA(0, 0, At, B0); PG8_MMA(0, 1, At, B1); } PG8_BAR; PG8_SCHED;
;             PG8_LDA(At, 1, 1); PG8_STAGE_B(PG8_SB(1, 0), b3); PG8_STAGE_B(PG8_SB(1, 1), b3 + hstepB); PG8_STAGE_A(PG8_SA(1, 0), a3, 0, gc);
;             PG8_WAIT_V(8); PG8_WAIT_L(0); PG8_BAR; if (cur.half != 1) { PG8_MMA(1, 0, At, B0); PG8_MMA(1, 1, At, B1); } PG8_BAR; PG8_SCHED;
.LBB0_1322:
	s_barrier
	v_add_u32_e32 v0, 0x18000, v216
	ds_read_b128 v[18:21], v0
	ds_read_b128 v[22:25], v0 offset:1024
	ds_read_b128 v[26:29], v0 offset:2048
	ds_read_b128 v[30:33], v0 offset:3072
	v_add_u32_e32 v0, 0x1c000, v216
	ds_read_b128 v[2:5], v0
	ds_read_b128 v[6:9], v0 offset:1024
	ds_read_b128 v[10:13], v0 offset:2048
	ds_read_b128 v[14:17], v0 offset:3072
	v_mov_b32_e32 v0, v214
	s_waitcnt lgkmcnt(0)
	ds_read_b128 v[58:61], v217 offset:32768
	ds_read_b128 v[62:65], v217 offset:33792
	ds_read_b128 v[50:53], v217 offset:34816
	ds_read_b128 v[54:57], v217 offset:35840
	ds_read_b128 v[42:45], v217 offset:36864
	ds_read_b128 v[46:49], v217 offset:37888
	ds_read_b128 v[34:37], v217 offset:38912
	ds_read_b128 v[38:41], v217 offset:39936
	s_mov_b32 m0, s77
	v_lshl_add_u64 v[194:195], s[42:43], 0, v[0:1]
	v_lshl_add_u64 v[194:195], v[194:195], 0, s[80:81]
	v_mov_b32_e32 v0, v214
	global_load_lds_dwordx4 v[194:195], off nt
	s_mov_b32 m0, s78
	v_lshl_add_u64 v[194:195], s[42:43], 0, v[0:1]
	v_lshl_add_u64 v[194:195], v[194:195], 0, s[82:83]
	global_load_lds_dwordx4 v[194:195], off nt
	s_waitcnt vmcnt(8)
	s_waitcnt lgkmcnt(0)
	s_and_b64 vcc, exec, s[4:5]
	s_barrier
	s_cbranch_vccnz .LBB0_1324
	s_setprio 1
	s_waitcnt lgkmcnt(0)
	v_mfma_f32_16x16x128_f8f6f4 v[190:193], v[18:25], v[58:65], v[190:193]
	v_mfma_f32_16x16x128_f8f6f4 v[186:189], v[26:33], v[58:65], v[186:189]
	v_mfma_f32_16x16x128_f8f6f4 v[182:185], v[18:25], v[50:57], v[182:185]
	v_mfma_f32_16x16x128_f8f6f4 v[178:181], v[26:33], v[50:57], v[178:181]
	v_mfma_f32_16x16x128_f8f6f4 v[158:161], v[18:25], v[42:49], v[158:161]
	v_mfma_f32_16x16x128_f8f6f4 v[154:157], v[26:33], v[42:49], v[154:157]
	v_mfma_f32_16x16x128_f8f6f4 v[150:153], v[18:25], v[34:41], v[150:153]
	v_mfma_f32_16x16x128_f8f6f4 v[146:149], v[26:33], v[34:41], v[146:149]
	s_setprio 0
	s_setprio 1
	v_mfma_f32_16x16x128_f8f6f4 v[174:177], v[2:9], v[58:65], v[174:177]
	v_mfma_f32_16x16x128_f8f6f4 v[170:173], v[10:17], v[58:65], v[170:173]
	v_mfma_f32_16x16x128_f8f6f4 v[166:169], v[2:9], v[50:57], v[166:169]
	v_mfma_f32_16x16x128_f8f6f4 v[162:165], v[10:17], v[50:57], v[162:165]
	v_mfma_f32_16x16x128_f8f6f4 v[142:145], v[2:9], v[42:49], v[142:145]
	v_mfma_f32_16x16x128_f8f6f4 v[138:141], v[10:17], v[42:49], v[138:141]
	v_mfma_f32_16x16x128_f8f6f4 v[134:137], v[2:9], v[34:41], v[134:137]
	v_mfma_f32_16x16x128_f8f6f4 v[130:133], v[10:17], v[34:41], v[130:133]
	s_setprio 0
.LBB0_1324:
	s_barrier
	v_mov_b32_e32 v0, v215
	s_waitcnt lgkmcnt(0)
	ds_read_b128 v[58:61], v217 offset:49152
	ds_read_b128 v[62:65], v217 offset:50176
	ds_read_b128 v[50:53], v217 offset:51200
	ds_read_b128 v[54:57], v217 offset:52224
	ds_read_b128 v[42:45], v217 offset:53248
	ds_read_b128 v[46:49], v217 offset:54272
	ds_read_b128 v[34:37], v217 offset:55296
	ds_read_b128 v[38:41], v217 offset:56320
	s_mov_b32 m0, s95
	v_lshl_add_u64 v[194:195], s[56:57], 0, v[0:1]
	v_lshl_add_u64 v[194:195], v[194:195], 0, s[84:85]
	v_mov_b32_e32 v0, v215
	global_load_lds_dwordx4 v[194:195], off
	s_mov_b32 m0, s97
	v_lshl_add_u64 v[194:195], s[56:57], 0, v[0:1]
	v_lshl_add_u64 v[194:195], v[194:195], 0, s[86:87]
	v_mov_b32_e32 v0, v215
	global_load_lds_dwordx4 v[194:195], off
	s_mov_b32 m0, s41
	v_lshl_add_u64 v[194:195], s[56:57], 0, v[0:1]
	v_lshl_add_u64 v[194:195], v[194:195], 0, s[88:89]
	v_mov_b32_e32 v0, v215
	global_load_lds_dwordx4 v[194:195], off
	s_mov_b32 m0, s44
	v_lshl_add_u64 v[194:195], s[56:57], 0, v[0:1]
	v_lshl_add_u64 v[194:195], v[194:195], 0, s[90:91]
	v_mov_b32_e32 v0, v214
	global_load_lds_dwordx4 v[194:195], off
	s_mov_b32 m0, s33
	v_lshl_add_u64 v[194:195], s[42:43], 0, v[0:1]
	v_lshl_add_u64 v[194:195], v[194:195], 0, s[84:85]
	v_mov_b32_e32 v0, v214
	global_load_lds_dwordx4 v[194:195], off nt
	s_mov_b32 m0, s38
	v_lshl_add_u64 v[194:195], s[42:43], 0, v[0:1]
	v_lshl_add_u64 v[194:195], v[194:195], 0, s[86:87]
	global_load_lds_dwordx4 v[194:195], off nt
	s_waitcnt vmcnt(8)
	s_waitcnt lgkmcnt(0)
	s_and_b64 vcc, exec, s[6:7]
	s_barrier
	s_cbranch_vccnz .LBB0_1310
	s_setprio 1
	s_waitcnt lgkmcnt(0)
	v_mfma_f32_16x16x128_f8f6f4 v[126:129], v[18:25], v[58:65], v[126:129]
	v_mfma_f32_16x16x128_f8f6f4 v[122:125], v[26:33], v[58:65], v[122:125]
	v_mfma_f32_16x16x128_f8f6f4 v[118:121], v[18:25], v[50:57], v[118:121]
	v_mfma_f32_16x16x128_f8f6f4 v[114:117], v[26:33], v[50:57], v[114:117]
	v_mfma_f32_16x16x128_f8f6f4 v[94:97], v[18:25], v[42:49], v[94:97]
	v_mfma_f32_16x16x128_f8f6f4 v[90:93], v[26:33], v[42:49], v[90:93]
	v_mfma_f32_16x16x128_f8f6f4 v[86:89], v[18:25], v[34:41], v[86:89]
	v_mfma_f32_16x16x128_f8f6f4 v[82:85], v[26:33], v[34:41], v[82:85]
	s_setprio 0
	s_setprio 1
	v_mfma_f32_16x16x128_f8f6f4 v[110:113], v[2:9], v[58:65], v[110:113]
	v_mfma_f32_16x16x128_f8f6f4 v[106:109], v[10:17], v[58:65], v[106:109]
	v_mfma_f32_16x16x128_f8f6f4 v[102:105], v[2:9], v[50:57], v[102:105]
	v_mfma_f32_16x16x128_f8f6f4 v[98:101], v[10:17], v[50:57], v[98:101]
	v_mfma_f32_16x16x128_f8f6f4 v[78:81], v[2:9], v[42:49], v[78:81]
	v_mfma_f32_16x16x128_f8f6f4 v[74:77], v[10:17], v[42:49], v[74:77]
	v_mfma_f32_16x16x128_f8f6f4 v[70:73], v[2:9], v[34:41], v[70:73]
	v_mfma_f32_16x16x128_f8f6f4 v[66:69], v[10:17], v[34:41], v[66:69]
	s_setprio 0
	s_branch .LBB0_1310
